# diff-attention QK^T: ds_read_b128 fragments software-pipelined 3-4 deep into registers that are dead outside PV (was read-wait-mfma per fragment)
# speedup vs baseline: 1.0184x; 1.0053x over previous
.LBB0_1354:
	v_cvt_f32_i32_e32 v130, v226
	v_mul_f32_e64 v0, -v190, v130
	s_mov_b32 s2, 0x41900000
	s_mov_b32 s3, 0x41980000
	v_pk_fma_f32 v[140:141], v[196:197], s[2:3], v[0:1] op_sel_hi:[1,1,0]
	s_mov_b32 s2, 0x41c00000
	s_mov_b32 s3, 0x41c80000
	v_pk_fma_f32 v[142:143], v[196:197], s[2:3], v[0:1] op_sel_hi:[1,1,0]
	s_mov_b32 s2, 0x41d00000
	s_mov_b32 s3, 0x41d80000
	v_pk_fma_f32 v[144:145], v[196:197], s[2:3], v[0:1] op_sel_hi:[1,1,0]
	s_mov_b32 s2, 0x42000000
	v_fma_f32 v131, -v190, v130, v190
	v_mov_b32_e32 v130, v0
	s_mov_b32 s3, 0x42040000
	v_fmac_f32_e32 v130, 0, v190
	v_pk_fma_f32 v[132:133], v[196:197], s[60:61], v[0:1] op_sel_hi:[1,1,0]
	v_pk_fma_f32 v[134:135], v[196:197], s[74:75], v[0:1] op_sel_hi:[1,1,0]
	v_pk_fma_f32 v[136:137], v[196:197], s[62:63], v[0:1] op_sel_hi:[1,1,0]
	v_pk_fma_f32 v[138:139], v[196:197], s[58:59], v[0:1] op_sel_hi:[1,1,0]
	v_pk_fma_f32 v[160:161], v[196:197], s[68:69], v[0:1] op_sel_hi:[1,1,0]
	v_pk_fma_f32 v[158:159], v[196:197], s[96:97], v[0:1] op_sel_hi:[1,1,0]
	v_pk_fma_f32 v[156:157], v[196:197], s[94:95], v[0:1] op_sel_hi:[1,1,0]
	v_pk_fma_f32 v[154:155], v[196:197], s[92:93], v[0:1] op_sel_hi:[1,1,0]
	v_pk_fma_f32 v[152:153], v[196:197], s[90:91], v[0:1] op_sel_hi:[1,1,0]
	v_pk_fma_f32 v[150:151], v[196:197], s[88:89], v[0:1] op_sel_hi:[1,1,0]
	v_pk_fma_f32 v[148:149], v[196:197], s[86:87], v[0:1] op_sel_hi:[1,1,0]
	v_pk_fma_f32 v[146:147], v[192:193], s[2:3], v[0:1] op_sel_hi:[1,1,0]
	s_setprio 1
	ds_read_b128 v[186:189], v205
	ds_read_b128 v[206:209], v205 offset:1024
	ds_read_b128 v[182:185], v224
	ds_read_b128 v[238:241], v224 offset:8192
	ds_read_b128 v[244:247], v223
	ds_read_b128 v[250:253], v223 offset:8192
	s_waitcnt lgkmcnt(3)
	v_mfma_f32_32x32x16_bf16 v[130:145], v[182:185], v[178:181], v[130:145]
	ds_read_b128 v[182:185], v222
	s_waitcnt lgkmcnt(3)
	v_mfma_f32_32x32x16_bf16 v[146:161], v[238:241], v[178:181], v[146:161]
	ds_read_b128 v[238:241], v222 offset:8192
	s_waitcnt lgkmcnt(3)
	v_mfma_f32_32x32x16_bf16 v[130:145], v[244:247], v[170:173], v[130:145]
	ds_read_b128 v[244:247], v221
	s_waitcnt lgkmcnt(3)
	v_mfma_f32_32x32x16_bf16 v[146:161], v[250:253], v[170:173], v[146:161]
	ds_read_b128 v[250:253], v221 offset:8192
	s_waitcnt lgkmcnt(3)
	v_mfma_f32_32x32x16_bf16 v[130:145], v[182:185], v[166:169], v[130:145]
	ds_read_b128 v[182:185], v224 offset:128
	s_waitcnt lgkmcnt(3)
	v_mfma_f32_32x32x16_bf16 v[146:161], v[238:241], v[166:169], v[146:161]
	ds_read_b128 v[238:241], v224 offset:8320
	s_waitcnt lgkmcnt(3)
	v_mfma_f32_32x32x16_bf16 v[130:145], v[244:247], v[162:165], v[130:145]
	ds_read_b128 v[244:247], v223 offset:128
	s_waitcnt lgkmcnt(3)
	v_mfma_f32_32x32x16_bf16 v[146:161], v[250:253], v[162:165], v[146:161]
	ds_read_b128 v[250:253], v223 offset:8320
	s_waitcnt lgkmcnt(3)
	v_mfma_f32_32x32x16_bf16 v[130:145], v[182:185], v[174:177], v[130:145]
	ds_read_b128 v[182:185], v222 offset:128
	s_waitcnt lgkmcnt(3)
	v_mfma_f32_32x32x16_bf16 v[146:161], v[238:241], v[174:177], v[146:161]
	ds_read_b128 v[238:241], v222 offset:8320
	s_waitcnt lgkmcnt(3)
	v_mfma_f32_32x32x16_bf16 v[130:145], v[244:247], v[186:189], v[130:145]
	ds_read_b128 v[244:247], v221 offset:128
	s_waitcnt lgkmcnt(3)
	v_mfma_f32_32x32x16_bf16 v[146:161], v[250:253], v[186:189], v[146:161]
	ds_read_b128 v[250:253], v221 offset:8320
	ds_read_b128 v[186:189], v205 offset:2048
	s_waitcnt lgkmcnt(4)
	v_mfma_f32_32x32x16_bf16 v[130:145], v[182:185], v[206:209], v[130:145]
	s_waitcnt lgkmcnt(3)
	v_mfma_f32_32x32x16_bf16 v[146:161], v[238:241], v[206:209], v[146:161]
	s_waitcnt lgkmcnt(0)
	v_mfma_f32_32x32x16_bf16 v[130:145], v[244:247], v[186:189], v[130:145]
	s_waitcnt lgkmcnt(0)
	v_mfma_f32_32x32x16_bf16 v[146:161], v[250:253], v[186:189], v[146:161]
	s_setprio 0
	s_add_i32 s2, s85, 0xffffff9f
	s_cmp_le_i32 s2, s65
	s_cbranch_scc1 .LBB0_1356
	v_cmp_gt_i32_e64 s[60:61], 26, v226
	v_cmp_gt_i32_e64 s[62:63], 27, v226
	v_cmp_gt_i32_e64 s[58:59], 25, v226
	s_and_b64 s[60:61], s[62:63], s[60:61]
	v_cmp_gt_i32_e64 s[56:57], 24, v226
	s_and_b64 s[58:59], s[60:61], s[58:59]
	v_cmp_gt_i32_e64 s[54:55], 19, v226
	s_and_b64 s[56:57], s[58:59], s[56:57]
	v_cmp_gt_i32_e64 s[52:53], 18, v226
	s_and_b64 s[54:55], s[56:57], s[54:55]
	v_cmp_gt_i32_e64 s[50:51], 17, v226
	s_and_b64 s[52:53], s[54:55], s[52:53]
	v_cmp_gt_i32_e64 s[48:49], 16, v226
	s_and_b64 s[50:51], s[52:53], s[50:51]
	v_cmp_gt_i32_e64 s[46:47], 11, v226
	s_and_b64 s[48:49], s[50:51], s[48:49]
	v_cmp_gt_i32_e64 s[44:45], 10, v226
	s_and_b64 s[46:47], s[48:49], s[46:47]
	v_cmp_gt_i32_e64 s[42:43], 9, v226
	s_and_b64 s[44:45], s[46:47], s[44:45]
	v_cmp_gt_i32_e64 s[40:41], 8, v226
	s_and_b64 s[42:43], s[44:45], s[42:43]
	v_cmp_gt_i32_e64 s[38:39], 3, v226
	s_and_b64 s[40:41], s[42:43], s[40:41]
	v_cmp_gt_i32_e64 s[36:37], 2, v226
	s_and_b64 s[38:39], s[40:41], s[38:39]
	v_cmp_gt_i32_e64 s[34:35], 1, v226
	s_and_b64 s[36:37], s[38:39], s[36:37]
	v_cmp_gt_i32_e64 s[30:31], 0, v226
	s_and_b64 s[34:35], s[36:37], s[34:35]
	s_and_b64 s[30:31], s[34:35], s[30:31]
	v_cmp_gt_i32_e64 s[28:29], 58, v226
	v_cndmask_b32_e64 v130, v130, v243, s[30:31]
	v_cmp_gt_i32_e64 s[30:31], 59, v226
	v_cmp_gt_i32_e64 s[26:27], 57, v226
	s_and_b64 s[28:29], s[30:31], s[28:29]
	v_cmp_gt_i32_e64 s[24:25], 56, v226
	s_and_b64 s[26:27], s[28:29], s[26:27]
	v_cmp_gt_i32_e64 s[22:23], 51, v226
	s_and_b64 s[24:25], s[26:27], s[24:25]
	v_cmp_gt_i32_e64 s[20:21], 50, v226
	s_and_b64 s[22:23], s[24:25], s[22:23]
	v_cmp_gt_i32_e64 s[18:19], 49, v226
	s_and_b64 s[20:21], s[22:23], s[20:21]
	v_cmp_gt_i32_e64 s[16:17], 48, v226
	s_and_b64 s[18:19], s[20:21], s[18:19]
	v_cmp_gt_i32_e64 s[14:15], 43, v226
	s_and_b64 s[16:17], s[18:19], s[16:17]
	v_cmp_gt_i32_e64 s[12:13], 42, v226
	s_and_b64 s[14:15], s[16:17], s[14:15]
	v_cmp_gt_i32_e64 s[10:11], 41, v226
	s_and_b64 s[12:13], s[14:15], s[12:13]
	v_cmp_gt_i32_e64 s[8:9], 40, v226
	s_and_b64 s[10:11], s[12:13], s[10:11]
	v_cmp_gt_i32_e64 s[6:7], 35, v226
	s_and_b64 s[8:9], s[10:11], s[8:9]
	v_cmp_gt_i32_e64 s[4:5], 34, v226
	s_and_b64 s[6:7], s[8:9], s[6:7]
	v_cmp_gt_i32_e64 s[2:3], 33, v226
	s_and_b64 s[4:5], s[6:7], s[4:5]
	v_cmp_gt_i32_e32 vcc, 32, v226
	s_and_b64 s[2:3], s[4:5], s[2:3]
	v_cndmask_b32_e64 v145, v145, v243, s[62:63]
	s_mov_b32 s62, 0x41200000
	v_cndmask_b32_e64 v144, v144, v243, s[60:61]
	s_mov_b32 s60, 2.0
	v_cndmask_b32_e64 v143, v143, v243, s[58:59]
	s_mov_b32 s58, 0x41800000
	s_and_b64 vcc, s[2:3], vcc
	s_mov_b32 s63, 0x41300000
	s_mov_b32 s61, 0x40400000
	s_mov_b32 s59, 0x41880000
	v_cndmask_b32_e64 v142, v142, v243, s[56:57]
	v_cndmask_b32_e64 v141, v141, v243, s[54:55]
	v_cndmask_b32_e64 v140, v140, v243, s[52:53]
	v_cndmask_b32_e64 v139, v139, v243, s[50:51]
	v_cndmask_b32_e64 v138, v138, v243, s[48:49]
	v_cndmask_b32_e64 v137, v137, v243, s[46:47]
	v_cndmask_b32_e64 v136, v136, v243, s[44:45]
	v_cndmask_b32_e64 v135, v135, v243, s[42:43]
	v_cndmask_b32_e64 v134, v134, v243, s[40:41]
	v_cndmask_b32_e64 v133, v133, v243, s[38:39]
	v_cndmask_b32_e64 v132, v132, v243, s[36:37]
	v_cndmask_b32_e64 v131, v131, v243, s[34:35]
	v_cndmask_b32_e64 v161, v161, v243, s[30:31]
	v_cndmask_b32_e64 v160, v160, v243, s[28:29]
	v_cndmask_b32_e64 v159, v159, v243, s[26:27]
	v_cndmask_b32_e64 v158, v158, v243, s[24:25]
	v_cndmask_b32_e64 v157, v157, v243, s[22:23]
	v_cndmask_b32_e64 v156, v156, v243, s[20:21]
	v_cndmask_b32_e64 v155, v155, v243, s[18:19]
	v_cndmask_b32_e64 v154, v154, v243, s[16:17]
	v_cndmask_b32_e64 v153, v153, v243, s[14:15]
	v_cndmask_b32_e64 v152, v152, v243, s[12:13]
	v_cndmask_b32_e64 v151, v151, v243, s[10:11]
	v_cndmask_b32_e64 v150, v150, v243, s[8:9]
	v_cndmask_b32_e64 v149, v149, v243, s[6:7]
	v_cndmask_b32_e64 v148, v148, v243, s[4:5]
	v_cndmask_b32_e64 v147, v147, v243, s[2:3]
	v_cndmask_b32_e32 v146, v146, v243, vcc

.LBB0_1360:
	v_lshl_add_u64 v[146:147], s[76:77], 0, v[194:195]
	v_add_co_u32_e32 v150, vcc, 0xc4000, v146
	v_lshl_add_u64 v[182:183], s[72:73], 0, v[194:195]
	s_nop 0
	v_addc_co_u32_e32 v151, vcc, 0, v147, vcc
	v_add_co_u32_e32 v154, vcc, 0x126000, v146
	s_nop 1
	v_addc_co_u32_e32 v155, vcc, 0, v147, vcc
	v_add_co_u32_e32 v184, vcc, 0xc4000, v182
	global_load_dwordx4 v[146:149], v[150:151], off
	s_nop 0
	global_load_dwordx4 v[150:153], v[150:151], off offset:256
	s_nop 0
	global_load_dwordx4 v[158:161], v[154:155], off
	s_nop 0
	global_load_dwordx4 v[154:157], v[154:155], off offset:256
	v_addc_co_u32_e32 v185, vcc, 0, v183, vcc
	v_add_co_u32_e32 v186, vcc, 0x126000, v182
	s_nop 1
	v_addc_co_u32_e32 v187, vcc, 0, v183, vcc
	global_load_dwordx4 v[182:185], v[184:185], off
	s_nop 0
	global_load_dwordx4 v[186:189], v[186:187], off
	s_setprio 1
	ds_read_b64_tr_b16 v[238:239], v213 offset:0
	ds_read_b64_tr_b16 v[240:241], v213 offset:0x1000
	ds_read_b64_tr_b16 v[244:245], v213 offset:0x2000
	ds_read_b64_tr_b16 v[246:247], v213 offset:0x3000
	ds_read_b64_tr_b16 v[250:251], v213 offset:0x4000
	ds_read_b64_tr_b16 v[252:253], v213 offset:0x5000
	ds_read_b64_tr_b16 v[206:207], v213 offset:0x6000
	ds_read_b64_tr_b16 v[208:209], v213 offset:0x7000
	s_waitcnt lgkmcnt(0)
	s_nop 0
	v_mfma_f32_32x32x16_bf16 v[114:129], v[130:133], v[238:241], v[114:129]
	v_mfma_f32_32x32x16_bf16 v[114:129], v[134:137], v[244:247], v[114:129]
	v_mfma_f32_32x32x16_bf16 v[114:129], v[138:141], v[250:253], v[114:129]
	v_mfma_f32_32x32x16_bf16 v[114:129], v[142:145], v[206:209], v[114:129]
	ds_read_b64_tr_b16 v[206:207], v213 offset:0x200
	ds_read_b64_tr_b16 v[208:209], v213 offset:0x1200
	ds_read_b64_tr_b16 v[238:239], v213 offset:0x2200
	ds_read_b64_tr_b16 v[240:241], v213 offset:0x3200
	ds_read_b64_tr_b16 v[244:245], v213 offset:0x4200
	ds_read_b64_tr_b16 v[246:247], v213 offset:0x5200
	ds_read_b64_tr_b16 v[250:251], v213 offset:0x6200
	ds_read_b64_tr_b16 v[252:253], v213 offset:0x7200
	s_waitcnt lgkmcnt(0)
	s_nop 0
	v_mfma_f32_32x32x16_bf16 v[98:113], v[130:133], v[206:209], v[98:113]
	ds_read_b64_tr_b16 v[206:207], v213 offset:0x400
	ds_read_b64_tr_b16 v[208:209], v213 offset:0x1400
	v_mfma_f32_32x32x16_bf16 v[98:113], v[134:137], v[238:241], v[98:113]
	ds_read_b64_tr_b16 v[238:239], v213 offset:0x2400
	ds_read_b64_tr_b16 v[240:241], v213 offset:0x3400
	v_mfma_f32_32x32x16_bf16 v[98:113], v[138:141], v[244:247], v[98:113]
	ds_read_b64_tr_b16 v[244:245], v213 offset:0x4400
	ds_read_b64_tr_b16 v[246:247], v213 offset:0x5400
	v_mfma_f32_32x32x16_bf16 v[98:113], v[142:145], v[250:253], v[98:113]
	ds_read_b64_tr_b16 v[250:251], v213 offset:0x6400
	ds_read_b64_tr_b16 v[252:253], v213 offset:0x7400
	s_waitcnt lgkmcnt(0)
	v_mfma_f32_32x32x16_bf16 v[82:97], v[130:133], v[206:209], v[82:97]
	ds_read_b64_tr_b16 v[206:207], v213 offset:0x600
	ds_read_b64_tr_b16 v[208:209], v213 offset:0x1600
	v_mfma_f32_32x32x16_bf16 v[82:97], v[134:137], v[238:241], v[82:97]
	ds_read_b64_tr_b16 v[238:239], v213 offset:0x2600
	ds_read_b64_tr_b16 v[240:241], v213 offset:0x3600
	v_mfma_f32_32x32x16_bf16 v[82:97], v[138:141], v[244:247], v[82:97]
	ds_read_b64_tr_b16 v[244:245], v213 offset:0x4600
	ds_read_b64_tr_b16 v[246:247], v213 offset:0x5600
	v_mfma_f32_32x32x16_bf16 v[82:97], v[142:145], v[250:253], v[82:97]
	ds_read_b64_tr_b16 v[250:251], v213 offset:0x6600
	ds_read_b64_tr_b16 v[252:253], v213 offset:0x7600
	s_waitcnt lgkmcnt(0)
	v_mfma_f32_32x32x16_bf16 v[66:81], v[130:133], v[206:209], v[66:81]
	ds_read_b64_tr_b16 v[206:207], v213 offset:0x800
	ds_read_b64_tr_b16 v[208:209], v213 offset:0x1800
	v_mfma_f32_32x32x16_bf16 v[66:81], v[134:137], v[238:241], v[66:81]
	ds_read_b64_tr_b16 v[238:239], v213 offset:0x2800
	ds_read_b64_tr_b16 v[240:241], v213 offset:0x3800
	v_mfma_f32_32x32x16_bf16 v[66:81], v[138:141], v[244:247], v[66:81]
	ds_read_b64_tr_b16 v[244:245], v213 offset:0x4800
	ds_read_b64_tr_b16 v[246:247], v213 offset:0x5800
	v_mfma_f32_32x32x16_bf16 v[66:81], v[142:145], v[250:253], v[66:81]
	ds_read_b64_tr_b16 v[250:251], v213 offset:0x6800
	ds_read_b64_tr_b16 v[252:253], v213 offset:0x7800
	s_waitcnt lgkmcnt(0)
	v_mfma_f32_32x32x16_bf16 v[50:65], v[130:133], v[206:209], v[50:65]
	ds_read_b64_tr_b16 v[206:207], v213 offset:0xa00
	ds_read_b64_tr_b16 v[208:209], v213 offset:0x1a00
	v_mfma_f32_32x32x16_bf16 v[50:65], v[134:137], v[238:241], v[50:65]
	ds_read_b64_tr_b16 v[238:239], v213 offset:0x2a00
	ds_read_b64_tr_b16 v[240:241], v213 offset:0x3a00
	v_mfma_f32_32x32x16_bf16 v[50:65], v[138:141], v[244:247], v[50:65]
	ds_read_b64_tr_b16 v[244:245], v213 offset:0x4a00
	ds_read_b64_tr_b16 v[246:247], v213 offset:0x5a00
	v_mfma_f32_32x32x16_bf16 v[50:65], v[142:145], v[250:253], v[50:65]
	ds_read_b64_tr_b16 v[250:251], v213 offset:0x6a00
	ds_read_b64_tr_b16 v[252:253], v213 offset:0x7a00
	s_waitcnt lgkmcnt(0)
	v_mfma_f32_32x32x16_bf16 v[34:49], v[130:133], v[206:209], v[34:49]
	ds_read_b64_tr_b16 v[206:207], v213 offset:0xc00
	ds_read_b64_tr_b16 v[208:209], v213 offset:0x1c00
	v_mfma_f32_32x32x16_bf16 v[34:49], v[134:137], v[238:241], v[34:49]
	ds_read_b64_tr_b16 v[238:239], v213 offset:0x2c00
	ds_read_b64_tr_b16 v[240:241], v213 offset:0x3c00
	v_mfma_f32_32x32x16_bf16 v[34:49], v[138:141], v[244:247], v[34:49]
	ds_read_b64_tr_b16 v[244:245], v213 offset:0x4c00
	ds_read_b64_tr_b16 v[246:247], v213 offset:0x5c00
	v_mfma_f32_32x32x16_bf16 v[34:49], v[142:145], v[250:253], v[34:49]
	ds_read_b64_tr_b16 v[250:251], v213 offset:0x6c00
	ds_read_b64_tr_b16 v[252:253], v213 offset:0x7c00
	s_waitcnt lgkmcnt(0)
	v_mfma_f32_32x32x16_bf16 v[18:33], v[130:133], v[206:209], v[18:33]
	ds_read_b64_tr_b16 v[206:207], v213 offset:0xe00
	ds_read_b64_tr_b16 v[208:209], v213 offset:0x1e00
	v_mfma_f32_32x32x16_bf16 v[18:33], v[134:137], v[238:241], v[18:33]
	ds_read_b64_tr_b16 v[238:239], v213 offset:0x2e00
	ds_read_b64_tr_b16 v[240:241], v213 offset:0x3e00
	v_mfma_f32_32x32x16_bf16 v[18:33], v[138:141], v[244:247], v[18:33]
	ds_read_b64_tr_b16 v[244:245], v213 offset:0x4e00
	ds_read_b64_tr_b16 v[246:247], v213 offset:0x5e00
	v_mfma_f32_32x32x16_bf16 v[18:33], v[142:145], v[250:253], v[18:33]
	ds_read_b64_tr_b16 v[250:251], v213 offset:0x6e00
	ds_read_b64_tr_b16 v[252:253], v213 offset:0x7e00
	s_waitcnt lgkmcnt(0)
	v_mfma_f32_32x32x16_bf16 v[2:17], v[130:133], v[206:209], v[2:17]
	v_mfma_f32_32x32x16_bf16 v[2:17], v[134:137], v[238:241], v[2:17]
	v_mfma_f32_32x32x16_bf16 v[2:17], v[138:141], v[244:247], v[2:17]
	v_mfma_f32_32x32x16_bf16 v[2:17], v[142:145], v[250:253], v[2:17]
	s_setprio 0
	v_add_u32_e32 v227, 0x14000, v225
	s_waitcnt vmcnt(0)
	s_waitcnt vmcnt(1)
	ds_write_b128 v227, v[182:185]
	s_waitcnt vmcnt(0)
	ds_write_b128 v227, v[186:189] offset:8192
	ds_write_b128 v220, v[146:149] offset:32768
	ds_write_b128 v220, v[158:161] offset:49152
	ds_write_b128 v220, v[150:153] offset:34816
	ds_write_b128 v220, v[154:157] offset:51200
	v_subrev_u32_e32 v182, 64, v226
	v_cvt_f32_i32_e32 v130, v182
	s_waitcnt lgkmcnt(0)
	s_barrier
	v_mul_f32_e64 v146, -v190, v130
	s_mov_b32 s2, 0x41900000
	s_mov_b32 s3, 0x41980000
	v_pk_fma_f32 v[140:141], v[196:197], s[2:3], v[146:147] op_sel_hi:[1,1,0]
	s_mov_b32 s2, 0x41c00000
	s_mov_b32 s3, 0x41c80000
	v_pk_fma_f32 v[142:143], v[196:197], s[2:3], v[146:147] op_sel_hi:[1,1,0]
	s_mov_b32 s2, 0x41d00000
	s_mov_b32 s3, 0x41d80000
	v_pk_fma_f32 v[144:145], v[196:197], s[2:3], v[146:147] op_sel_hi:[1,1,0]
	s_mov_b32 s2, 0x42000000
	v_fma_f32 v131, -v190, v130, v190
	v_mov_b32_e32 v130, v146
	v_mov_b32_e32 v191, v190
	s_mov_b32 s3, 0x42040000
	v_fmac_f32_e32 v130, 0, v190
	v_pk_fma_f32 v[132:133], v[196:197], s[60:61], v[146:147] op_sel_hi:[1,1,0]
	v_pk_fma_f32 v[134:135], v[196:197], s[74:75], v[146:147] op_sel_hi:[1,1,0]
	v_pk_fma_f32 v[136:137], v[196:197], s[62:63], v[146:147] op_sel_hi:[1,1,0]
	v_pk_fma_f32 v[138:139], v[196:197], s[58:59], v[146:147] op_sel_hi:[1,1,0]
	v_pk_fma_f32 v[160:161], v[190:191], s[68:69], v[146:147] op_sel_hi:[1,1,0]
	v_pk_fma_f32 v[158:159], v[190:191], s[96:97], v[146:147] op_sel_hi:[1,1,0]
	v_pk_fma_f32 v[156:157], v[190:191], s[94:95], v[146:147] op_sel_hi:[1,1,0]
	v_pk_fma_f32 v[154:155], v[190:191], s[92:93], v[146:147] op_sel_hi:[1,1,0]
	v_pk_fma_f32 v[152:153], v[190:191], s[90:91], v[146:147] op_sel_hi:[1,1,0]
	v_pk_fma_f32 v[150:151], v[190:191], s[88:89], v[146:147] op_sel_hi:[1,1,0]
	v_pk_fma_f32 v[148:149], v[190:191], s[86:87], v[146:147] op_sel_hi:[1,1,0]
	v_pk_fma_f32 v[146:147], v[192:193], s[2:3], v[146:147] op_sel_hi:[1,1,0]
	s_setprio 1
	ds_read_b128 v[206:209], v205
	ds_read_b128 v[250:253], v205 offset:1024
	ds_read_b128 v[184:187], v218
	ds_read_b128 v[238:241], v218 offset:8192
	ds_read_b128 v[244:247], v217
	s_waitcnt lgkmcnt(2)
	v_mfma_f32_32x32x16_bf16 v[130:145], v[184:187], v[178:181], v[130:145]
	ds_read_b128 v[184:187], v217 offset:8192
	s_waitcnt lgkmcnt(2)
	v_mfma_f32_32x32x16_bf16 v[146:161], v[238:241], v[178:181], v[146:161]
	ds_read_b128 v[238:241], v216
	s_waitcnt lgkmcnt(2)
	v_mfma_f32_32x32x16_bf16 v[130:145], v[244:247], v[170:173], v[130:145]
	ds_read_b128 v[244:247], v216 offset:8192
	s_waitcnt lgkmcnt(2)
	v_mfma_f32_32x32x16_bf16 v[146:161], v[184:187], v[170:173], v[146:161]
	ds_read_b128 v[184:187], v215
	s_waitcnt lgkmcnt(2)
	v_mfma_f32_32x32x16_bf16 v[130:145], v[238:241], v[166:169], v[130:145]
	ds_read_b128 v[238:241], v215 offset:8192
	s_waitcnt lgkmcnt(2)
	v_mfma_f32_32x32x16_bf16 v[146:161], v[244:247], v[166:169], v[146:161]
	ds_read_b128 v[244:247], v218 offset:128
	s_waitcnt lgkmcnt(2)
	v_mfma_f32_32x32x16_bf16 v[130:145], v[184:187], v[162:165], v[130:145]
	ds_read_b128 v[184:187], v218 offset:8320
	s_waitcnt lgkmcnt(2)
	v_mfma_f32_32x32x16_bf16 v[146:161], v[238:241], v[162:165], v[146:161]
	ds_read_b128 v[238:241], v217 offset:128
	s_waitcnt lgkmcnt(2)
	v_mfma_f32_32x32x16_bf16 v[130:145], v[244:247], v[174:177], v[130:145]
	ds_read_b128 v[244:247], v217 offset:8320
	s_waitcnt lgkmcnt(2)
	v_mfma_f32_32x32x16_bf16 v[146:161], v[184:187], v[174:177], v[146:161]
	ds_read_b128 v[184:187], v216 offset:128
	s_waitcnt lgkmcnt(2)
	v_mfma_f32_32x32x16_bf16 v[130:145], v[238:241], v[206:209], v[130:145]
	ds_read_b128 v[238:241], v216 offset:8320
	s_waitcnt lgkmcnt(2)
	v_mfma_f32_32x32x16_bf16 v[146:161], v[244:247], v[206:209], v[146:161]
	ds_read_b128 v[244:247], v215 offset:128
	ds_read_b128 v[206:209], v205 offset:2048
	s_waitcnt lgkmcnt(3)
	v_mfma_f32_32x32x16_bf16 v[130:145], v[184:187], v[250:253], v[130:145]
	ds_read_b128 v[184:187], v215 offset:8320
	s_waitcnt lgkmcnt(3)
	v_mfma_f32_32x32x16_bf16 v[146:161], v[238:241], v[250:253], v[146:161]
	s_waitcnt lgkmcnt(1)
	v_mfma_f32_32x32x16_bf16 v[130:145], v[244:247], v[206:209], v[130:145]
	s_waitcnt lgkmcnt(0)
	v_mfma_f32_32x32x16_bf16 v[146:161], v[184:187], v[206:209], v[146:161]
	s_setprio 0
	s_sub_i32 s2, s85, 33
	s_cmp_le_i32 s2, s65
	s_cbranch_scc1 .LBB0_1362
	v_cmp_gt_i32_e64 s[60:61], 26, v182
	v_cmp_gt_i32_e64 s[62:63], 27, v182
	v_cmp_gt_i32_e64 s[58:59], 25, v182
	s_and_b64 s[60:61], s[62:63], s[60:61]
	v_cmp_gt_i32_e64 s[56:57], 24, v182
	s_and_b64 s[58:59], s[60:61], s[58:59]
	v_cmp_gt_i32_e64 s[54:55], 19, v182
	s_and_b64 s[56:57], s[58:59], s[56:57]
	v_cmp_gt_i32_e64 s[52:53], 18, v182
	s_and_b64 s[54:55], s[56:57], s[54:55]
	v_cmp_gt_i32_e64 s[50:51], 17, v182
	s_and_b64 s[52:53], s[54:55], s[52:53]
	v_cmp_gt_i32_e64 s[48:49], 16, v182
	s_and_b64 s[50:51], s[52:53], s[50:51]
	v_cmp_gt_i32_e64 s[46:47], 11, v182
	s_and_b64 s[48:49], s[50:51], s[48:49]
	v_cmp_gt_i32_e64 s[44:45], 10, v182
	s_and_b64 s[46:47], s[48:49], s[46:47]
	v_cmp_gt_i32_e64 s[42:43], 9, v182
	s_and_b64 s[44:45], s[46:47], s[44:45]
	v_cmp_gt_i32_e64 s[40:41], 8, v182
	s_and_b64 s[42:43], s[44:45], s[42:43]
	v_cmp_gt_i32_e64 s[38:39], 3, v182
	s_and_b64 s[40:41], s[42:43], s[40:41]
	v_cmp_gt_i32_e64 s[36:37], 2, v182
	s_and_b64 s[38:39], s[40:41], s[38:39]
	v_cmp_gt_i32_e64 s[34:35], 1, v182
	s_and_b64 s[36:37], s[38:39], s[36:37]
	v_cmp_gt_i32_e64 s[30:31], 0, v182
	s_and_b64 s[34:35], s[36:37], s[34:35]
	s_and_b64 s[30:31], s[34:35], s[30:31]
	v_cmp_gt_i32_e64 s[28:29], 58, v182
	v_cndmask_b32_e64 v130, v130, v243, s[30:31]
	v_cmp_gt_i32_e64 s[30:31], 59, v182
	v_cmp_gt_i32_e64 s[26:27], 57, v182
	s_and_b64 s[28:29], s[30:31], s[28:29]
	v_cmp_gt_i32_e64 s[24:25], 56, v182
	s_and_b64 s[26:27], s[28:29], s[26:27]
	v_cmp_gt_i32_e64 s[22:23], 51, v182
	s_and_b64 s[24:25], s[26:27], s[24:25]
	v_cmp_gt_i32_e64 s[20:21], 50, v182
	s_and_b64 s[22:23], s[24:25], s[22:23]
	v_cmp_gt_i32_e64 s[18:19], 49, v182
	s_and_b64 s[20:21], s[22:23], s[20:21]
	v_cmp_gt_i32_e64 s[16:17], 48, v182
	s_and_b64 s[18:19], s[20:21], s[18:19]
	v_cmp_gt_i32_e64 s[14:15], 43, v182
	s_and_b64 s[16:17], s[18:19], s[16:17]
	v_cmp_gt_i32_e64 s[12:13], 42, v182
	s_and_b64 s[14:15], s[16:17], s[14:15]
	v_cmp_gt_i32_e64 s[10:11], 41, v182
	s_and_b64 s[12:13], s[14:15], s[12:13]
	v_cmp_gt_i32_e64 s[8:9], 40, v182
	s_and_b64 s[10:11], s[12:13], s[10:11]
	v_cmp_gt_i32_e64 s[6:7], 35, v182
	s_and_b64 s[8:9], s[10:11], s[8:9]
	v_cmp_gt_i32_e64 s[4:5], 34, v182
	s_and_b64 s[6:7], s[8:9], s[6:7]
	v_cmp_gt_i32_e64 s[2:3], 33, v182
	s_and_b64 s[4:5], s[6:7], s[4:5]
	v_cmp_gt_i32_e32 vcc, 32, v182
	s_and_b64 s[2:3], s[4:5], s[2:3]
	v_cndmask_b32_e64 v145, v145, v243, s[62:63]
	s_mov_b32 s62, 0x41200000
	v_cndmask_b32_e64 v144, v144, v243, s[60:61]
	s_mov_b32 s60, 2.0
	v_cndmask_b32_e64 v143, v143, v243, s[58:59]
	s_mov_b32 s58, 0x41800000
	s_and_b64 vcc, s[2:3], vcc
	s_mov_b32 s63, 0x41300000
	s_mov_b32 s61, 0x40400000
	s_mov_b32 s59, 0x41880000
	v_cndmask_b32_e64 v142, v142, v243, s[56:57]
	v_cndmask_b32_e64 v141, v141, v243, s[54:55]
	v_cndmask_b32_e64 v140, v140, v243, s[52:53]
	v_cndmask_b32_e64 v139, v139, v243, s[50:51]
	v_cndmask_b32_e64 v138, v138, v243, s[48:49]
	v_cndmask_b32_e64 v137, v137, v243, s[46:47]
	v_cndmask_b32_e64 v136, v136, v243, s[44:45]
	v_cndmask_b32_e64 v135, v135, v243, s[42:43]
	v_cndmask_b32_e64 v134, v134, v243, s[40:41]
	v_cndmask_b32_e64 v133, v133, v243, s[38:39]
	v_cndmask_b32_e64 v132, v132, v243, s[36:37]
	v_cndmask_b32_e64 v131, v131, v243, s[34:35]
	v_cndmask_b32_e64 v161, v161, v243, s[30:31]
	v_cndmask_b32_e64 v160, v160, v243, s[28:29]
	v_cndmask_b32_e64 v159, v159, v243, s[26:27]
	v_cndmask_b32_e64 v158, v158, v243, s[24:25]
	v_cndmask_b32_e64 v157, v157, v243, s[22:23]
	v_cndmask_b32_e64 v156, v156, v243, s[20:21]
	v_cndmask_b32_e64 v155, v155, v243, s[18:19]
	v_cndmask_b32_e64 v154, v154, v243, s[16:17]
	v_cndmask_b32_e64 v153, v153, v243, s[14:15]
	v_cndmask_b32_e64 v152, v152, v243, s[12:13]
	v_cndmask_b32_e64 v151, v151, v243, s[10:11]
	v_cndmask_b32_e64 v150, v150, v243, s[8:9]
	v_cndmask_b32_e64 v149, v149, v243, s[6:7]
	v_cndmask_b32_e64 v148, v148, v243, s[4:5]
	v_cndmask_b32_e64 v147, v147, v243, s[2:3]
	v_cndmask_b32_e32 v146, v146, v243, vcc

.LBB0_1365:
	s_and_b32 s72, s83, 0xffffffc0
	v_subrev_u32_e32 v130, s72, v219
	v_add_u32_e32 v182, 0x80, v130
	v_cvt_f32_i32_e32 v130, v182
	v_mul_f32_e64 v146, -v190, v130
	s_mov_b32 s2, 0x41900000
	s_mov_b32 s3, 0x41980000
	v_pk_fma_f32 v[140:141], v[196:197], s[2:3], v[146:147] op_sel_hi:[1,1,0]
	s_mov_b32 s2, 0x41c00000
	s_mov_b32 s3, 0x41c80000
	v_pk_fma_f32 v[142:143], v[196:197], s[2:3], v[146:147] op_sel_hi:[1,1,0]
	s_mov_b32 s2, 0x41d00000
	s_mov_b32 s3, 0x41d80000
	v_pk_fma_f32 v[144:145], v[196:197], s[2:3], v[146:147] op_sel_hi:[1,1,0]
	s_mov_b32 s2, 0x42000000
	v_fma_f32 v131, -v190, v130, v190
	v_mov_b32_e32 v130, v146
	v_mov_b32_e32 v191, v190
	s_mov_b32 s3, 0x42040000
	v_fmac_f32_e32 v130, 0, v190
	v_pk_fma_f32 v[132:133], v[196:197], s[60:61], v[146:147] op_sel_hi:[1,1,0]
	v_pk_fma_f32 v[134:135], v[196:197], s[74:75], v[146:147] op_sel_hi:[1,1,0]
	v_pk_fma_f32 v[136:137], v[196:197], s[62:63], v[146:147] op_sel_hi:[1,1,0]
	v_pk_fma_f32 v[138:139], v[196:197], s[58:59], v[146:147] op_sel_hi:[1,1,0]
	v_pk_fma_f32 v[160:161], v[190:191], s[68:69], v[146:147] op_sel_hi:[1,1,0]
	v_pk_fma_f32 v[158:159], v[190:191], s[96:97], v[146:147] op_sel_hi:[1,1,0]
	v_pk_fma_f32 v[156:157], v[190:191], s[94:95], v[146:147] op_sel_hi:[1,1,0]
	v_pk_fma_f32 v[154:155], v[190:191], s[92:93], v[146:147] op_sel_hi:[1,1,0]
	v_pk_fma_f32 v[152:153], v[190:191], s[90:91], v[146:147] op_sel_hi:[1,1,0]
	v_pk_fma_f32 v[150:151], v[190:191], s[88:89], v[146:147] op_sel_hi:[1,1,0]
	v_pk_fma_f32 v[148:149], v[190:191], s[86:87], v[146:147] op_sel_hi:[1,1,0]
	v_pk_fma_f32 v[146:147], v[192:193], s[2:3], v[146:147] op_sel_hi:[1,1,0]
	s_setprio 1
	ds_read_b128 v[198:201], v205
	ds_read_b128 v[206:209], v205 offset:1024
	ds_read_b128 v[184:187], v224
	ds_read_b128 v[238:241], v224 offset:8192
	ds_read_b128 v[244:247], v223
	ds_read_b128 v[250:253], v223 offset:8192
	s_waitcnt lgkmcnt(3)
	v_mfma_f32_32x32x16_bf16 v[130:145], v[184:187], v[178:181], v[130:145]
	ds_read_b128 v[184:187], v222
	s_waitcnt lgkmcnt(3)
	v_mfma_f32_32x32x16_bf16 v[146:161], v[238:241], v[178:181], v[146:161]
	ds_read_b128 v[238:241], v222 offset:8192
	s_waitcnt lgkmcnt(3)
	v_mfma_f32_32x32x16_bf16 v[130:145], v[244:247], v[170:173], v[130:145]
	ds_read_b128 v[244:247], v221
	s_waitcnt lgkmcnt(3)
	v_mfma_f32_32x32x16_bf16 v[146:161], v[250:253], v[170:173], v[146:161]
	ds_read_b128 v[250:253], v221 offset:8192
	s_waitcnt lgkmcnt(3)
	v_mfma_f32_32x32x16_bf16 v[130:145], v[184:187], v[166:169], v[130:145]
	ds_read_b128 v[184:187], v224 offset:128
	s_waitcnt lgkmcnt(3)
	v_mfma_f32_32x32x16_bf16 v[146:161], v[238:241], v[166:169], v[146:161]
	ds_read_b128 v[238:241], v224 offset:8320
	s_waitcnt lgkmcnt(3)
	v_mfma_f32_32x32x16_bf16 v[130:145], v[244:247], v[162:165], v[130:145]
	ds_read_b128 v[244:247], v223 offset:128
	s_waitcnt lgkmcnt(3)
	v_mfma_f32_32x32x16_bf16 v[146:161], v[250:253], v[162:165], v[146:161]
	ds_read_b128 v[250:253], v223 offset:8320
	s_waitcnt lgkmcnt(3)
	v_mfma_f32_32x32x16_bf16 v[130:145], v[184:187], v[174:177], v[130:145]
	ds_read_b128 v[184:187], v222 offset:128
	s_waitcnt lgkmcnt(3)
	v_mfma_f32_32x32x16_bf16 v[146:161], v[238:241], v[174:177], v[146:161]
	ds_read_b128 v[238:241], v222 offset:8320
	s_waitcnt lgkmcnt(3)
	v_mfma_f32_32x32x16_bf16 v[130:145], v[244:247], v[198:201], v[130:145]
	ds_read_b128 v[244:247], v221 offset:128
	s_waitcnt lgkmcnt(3)
	v_mfma_f32_32x32x16_bf16 v[146:161], v[250:253], v[198:201], v[146:161]
	ds_read_b128 v[250:253], v221 offset:8320
	ds_read_b128 v[198:201], v205 offset:2048
	s_waitcnt lgkmcnt(4)
	v_mfma_f32_32x32x16_bf16 v[130:145], v[184:187], v[206:209], v[130:145]
	s_waitcnt lgkmcnt(3)
	v_mfma_f32_32x32x16_bf16 v[146:161], v[238:241], v[206:209], v[146:161]
	s_waitcnt lgkmcnt(0)
	v_mfma_f32_32x32x16_bf16 v[130:145], v[244:247], v[198:201], v[130:145]
	s_waitcnt lgkmcnt(0)
	v_mfma_f32_32x32x16_bf16 v[146:161], v[250:253], v[198:201], v[146:161]
	s_setprio 0
	s_add_i32 s2, s72, 0xffffffbf
	s_cmp_gt_i32 s2, s65
	s_cbranch_scc0 .LBB0_1367
	v_cmp_gt_i32_e64 s[60:61], 26, v182
	v_cmp_gt_i32_e64 s[62:63], 27, v182
	v_cmp_gt_i32_e64 s[58:59], 25, v182
	s_and_b64 s[60:61], s[62:63], s[60:61]
	v_cmp_gt_i32_e64 s[56:57], 24, v182
	s_and_b64 s[58:59], s[60:61], s[58:59]
	v_cmp_gt_i32_e64 s[54:55], 19, v182
	s_and_b64 s[56:57], s[58:59], s[56:57]
	v_cmp_gt_i32_e64 s[52:53], 18, v182
	s_and_b64 s[54:55], s[56:57], s[54:55]
	v_cmp_gt_i32_e64 s[50:51], 17, v182
	s_and_b64 s[52:53], s[54:55], s[52:53]
	v_cmp_gt_i32_e64 s[48:49], 16, v182
	s_and_b64 s[50:51], s[52:53], s[50:51]
	v_cmp_gt_i32_e64 s[46:47], 11, v182
	s_and_b64 s[48:49], s[50:51], s[48:49]
	v_cmp_gt_i32_e64 s[44:45], 10, v182
	s_and_b64 s[46:47], s[48:49], s[46:47]
	v_cmp_gt_i32_e64 s[42:43], 9, v182
	s_and_b64 s[44:45], s[46:47], s[44:45]
	v_cmp_gt_i32_e64 s[40:41], 8, v182
	s_and_b64 s[42:43], s[44:45], s[42:43]
	v_cmp_gt_i32_e64 s[38:39], 3, v182
	s_and_b64 s[40:41], s[42:43], s[40:41]
	v_cmp_gt_i32_e64 s[36:37], 2, v182
	s_and_b64 s[38:39], s[40:41], s[38:39]
	v_cmp_gt_i32_e64 s[34:35], 1, v182
	s_and_b64 s[36:37], s[38:39], s[36:37]
	v_cmp_gt_i32_e64 s[30:31], 0, v182
	s_and_b64 s[34:35], s[36:37], s[34:35]
	s_and_b64 s[30:31], s[34:35], s[30:31]
	v_cmp_gt_i32_e64 s[28:29], 58, v182
	v_cndmask_b32_e64 v130, v130, v243, s[30:31]
	v_cmp_gt_i32_e64 s[30:31], 59, v182
	v_cmp_gt_i32_e64 s[26:27], 57, v182
	s_and_b64 s[28:29], s[30:31], s[28:29]
	v_cmp_gt_i32_e64 s[24:25], 56, v182
	s_and_b64 s[26:27], s[28:29], s[26:27]
	v_cmp_gt_i32_e64 s[22:23], 51, v182
	s_and_b64 s[24:25], s[26:27], s[24:25]
	v_cmp_gt_i32_e64 s[20:21], 50, v182
	s_and_b64 s[22:23], s[24:25], s[22:23]
	v_cmp_gt_i32_e64 s[18:19], 49, v182
	s_and_b64 s[20:21], s[22:23], s[20:21]
	v_cmp_gt_i32_e64 s[16:17], 48, v182
	s_and_b64 s[18:19], s[20:21], s[18:19]
	v_cmp_gt_i32_e64 s[14:15], 43, v182
	s_and_b64 s[16:17], s[18:19], s[16:17]
	v_cmp_gt_i32_e64 s[12:13], 42, v182
	s_and_b64 s[14:15], s[16:17], s[14:15]
	v_cmp_gt_i32_e64 s[10:11], 41, v182
	s_and_b64 s[12:13], s[14:15], s[12:13]
	v_cmp_gt_i32_e64 s[8:9], 40, v182
	s_and_b64 s[10:11], s[12:13], s[10:11]
	v_cmp_gt_i32_e64 s[6:7], 35, v182
	s_and_b64 s[8:9], s[10:11], s[8:9]
	v_cmp_gt_i32_e64 s[4:5], 34, v182
	s_and_b64 s[6:7], s[8:9], s[6:7]
	v_cmp_gt_i32_e64 s[2:3], 33, v182
	s_and_b64 s[4:5], s[6:7], s[4:5]
	v_cmp_gt_i32_e32 vcc, 32, v182
	s_and_b64 s[2:3], s[4:5], s[2:3]
	v_cndmask_b32_e64 v145, v145, v243, s[62:63]
	s_mov_b32 s62, 0x41200000
	v_cndmask_b32_e64 v144, v144, v243, s[60:61]
	s_mov_b32 s60, 2.0
	v_cndmask_b32_e64 v143, v143, v243, s[58:59]
	s_mov_b32 s58, 0x41800000
	s_and_b64 vcc, s[2:3], vcc
	s_mov_b32 s63, 0x41300000
	s_mov_b32 s61, 0x40400000
	s_mov_b32 s59, 0x41880000
	v_cndmask_b32_e64 v142, v142, v243, s[56:57]
	v_cndmask_b32_e64 v141, v141, v243, s[54:55]
	v_cndmask_b32_e64 v140, v140, v243, s[52:53]
	v_cndmask_b32_e64 v139, v139, v243, s[50:51]
	v_cndmask_b32_e64 v138, v138, v243, s[48:49]
	v_cndmask_b32_e64 v137, v137, v243, s[46:47]
	v_cndmask_b32_e64 v136, v136, v243, s[44:45]
	v_cndmask_b32_e64 v135, v135, v243, s[42:43]
	v_cndmask_b32_e64 v134, v134, v243, s[40:41]
	v_cndmask_b32_e64 v133, v133, v243, s[38:39]
	v_cndmask_b32_e64 v132, v132, v243, s[36:37]
	v_cndmask_b32_e64 v131, v131, v243, s[34:35]
	v_cndmask_b32_e64 v161, v161, v243, s[30:31]
	v_cndmask_b32_e64 v160, v160, v243, s[28:29]
	v_cndmask_b32_e64 v159, v159, v243, s[26:27]
	v_cndmask_b32_e64 v158, v158, v243, s[24:25]
	v_cndmask_b32_e64 v157, v157, v243, s[22:23]
	v_cndmask_b32_e64 v156, v156, v243, s[20:21]
	v_cndmask_b32_e64 v155, v155, v243, s[18:19]
	v_cndmask_b32_e64 v154, v154, v243, s[16:17]
	v_cndmask_b32_e64 v153, v153, v243, s[14:15]
	v_cndmask_b32_e64 v152, v152, v243, s[12:13]
	v_cndmask_b32_e64 v151, v151, v243, s[10:11]
	v_cndmask_b32_e64 v150, v150, v243, s[8:9]
	v_cndmask_b32_e64 v149, v149, v243, s[6:7]
	v_cndmask_b32_e64 v148, v148, v243, s[4:5]
	v_cndmask_b32_e64 v147, v147, v243, s[2:3]
	v_cndmask_b32_e32 v146, v146, v243, vcc
